# baseline (speedup 1.0000x reference)
_ZN12_GLOBAL__N_17k_pairsEPKDF16_PKiS1_PKfS5_S5_Pf:
	s_cmpk_gt_u32 s2, 0x2ff
	s_cbranch_scc1 .Lpairs_exit
	s_load_dwordx8 s[4:11], s[0:1], 0x0
	s_load_dwordx4 s[12:15], s[0:1], 0x20
	s_load_dwordx2 s[16:17], s[0:1], 0x30
	v_lshrrev_b32_e32 v2, 6, v0
	v_and_b32_e32 v1, 15, v0
	v_lshlrev_b32_e32 v72, 4, v0
	v_readfirstlane_b32 s3, v2
	s_lshl_b32 s32, s2, 3
	s_add_i32 s32, s32, s3
	s_add_i32 s33, s32, 0x1800
	s_add_i32 s34, s2, 0x3000
	s_cmp_lg_u32 s3, 0
	s_cselect_b32 s34, 0x7fff, s34
	v_lshlrev_b32_e32 v77, 3, v1
	v_add_u32_e32 v73, 0x2000, v72
	v_and_b32_e32 v76, 48, v0
	v_lshlrev_b32_e32 v3, 2, v1
	s_waitcnt lgkmcnt(0)
	s_min_i32 s3, s32, 0x30d3
	s_lshl_b32 s3, s3, 7
	s_add_u32 s24, s6, s3
	s_addc_u32 s25, s7, 0
	global_load_dwordx2 v[68:69], v77, s[24:25] nt
	s_min_i32 s3, s33, 0x30d3
	s_lshl_b32 s3, s3, 7
	s_add_u32 s24, s6, s3
	s_addc_u32 s25, s7, 0
	global_load_dwordx2 v[74:75], v77, s[24:25] nt
	global_load_dwordx4 v[52:55], v72, s[8:9]
	global_load_dwordx4 v[56:59], v73, s[8:9]
	s_load_dword s18, s[14:15], 0x0
	global_load_dword v4, v3, s[12:13] offset:0
	global_load_dword v8, v3, s[10:11] offset:0
	global_load_dword v5, v3, s[12:13] offset:64
	global_load_dword v9, v3, s[10:11] offset:64
	global_load_dword v6, v3, s[12:13] offset:128
	global_load_dword v10, v3, s[10:11] offset:128
	global_load_dword v7, v3, s[12:13] offset:192
	global_load_dword v11, v3, s[10:11] offset:192
	v_and_b32_e32 v2, 63, v0
	v_lshlrev_b32_e32 v2, 4, v2
	v_cmp_eq_u32_e64 s[20:21], 1, v1
	v_cmp_eq_u32_e64 s[22:23], 2, v1
	v_cmp_eq_u32_e64 s[26:27], 3, v1
	v_cmp_gt_u32_e64 s[28:29], 4, v1
	v_add_u32_e32 v0, v76, v3
	s_waitcnt vmcnt(10)
	v_lshl_or_b32 v70, v68, 7, v76
	v_lshl_or_b32 v71, v69, 7, v76
	global_load_dwordx4 v[20:23], v70, s[4:5]
	global_load_dwordx4 v[24:27], v70, s[4:5] offset:64
	global_load_dwordx4 v[28:31], v71, s[4:5]
	global_load_dwordx4 v[32:35], v71, s[4:5] offset:64
	v_lshl_or_b32 v70, v74, 7, v76
	v_lshl_or_b32 v71, v75, 7, v76
	global_load_dwordx4 v[36:39], v70, s[4:5]
	global_load_dwordx4 v[40:43], v70, s[4:5] offset:64
	global_load_dwordx4 v[44:47], v71, s[4:5]
	global_load_dwordx4 v[48:51], v71, s[4:5] offset:64
	s_cmpk_lt_i32 s34, 0x30d4
	s_cbranch_scc0 .Lpairs_no3a
	s_min_i32 s3, s34, 0x30d3
	s_lshl_b32 s3, s3, 7
	s_add_u32 s24, s6, s3
	s_addc_u32 s25, s7, 0
	global_load_dwordx2 v[68:69], v77, s[24:25] nt
